# scan phase: counted LDS waits, o-stores no longer waited on per step, branch-free LDS-DMA address generation
# speedup vs baseline: 1.0086x; 1.0086x over previous
.LBB0_713:
	v_lshl_add_u64 v[68:69], s[6:7], 0, v[130:131]
	v_readlane_b32 s6, v252, 44
	v_readlane_b32 s7, v252, 45
	s_lshl_b32 s48, s36, 10
	s_add_i32 m0, s48, 0
	s_and_b32 s12, s14, 1
	global_load_lds_dwordx4 v[68:69], off
	s_nop 0
	global_load_dword v134, v131, s[6:7]
	s_or_b32 s74, s12, s44
	s_cmp_lt_i32 s14, 2
	s_cselect_b64 s[6:7], -1, 0
	s_sub_i32 s52, s16, 51
	s_lshr_b32 s52, s52, 3
	s_add_i32 s52, s52, s44
	s_sub_i32 s12, s16, 56
	s_lshl_b32 s68, s52, 11
	s_sub_i32 s52, s16, 50
	s_lshr_b32 s12, s12, 3
	s_lshr_b32 s52, s52, 3
	s_add_i32 s12, s12, s44
	s_add_i32 s52, s52, s44
	s_lshl_b32 s49, s14, 13
	s_lshl_b32 s40, s12, 11
	s_sub_i32 s12, s16, 55
	s_sub_i32 s14, s16, 54
	s_sub_i32 s42, s16, 53
	s_sub_i32 s46, s16, 52
	s_lshl_b32 s70, s52, 11
	s_sub_i32 s52, s16, 49
	s_lshr_b32 s12, s12, 3
	s_lshr_b32 s14, s14, 3
	s_lshr_b32 s42, s42, 3
	s_lshr_b32 s46, s46, 3
	s_lshr_b32 s52, s52, 3
	s_mov_b32 s41, s79
	s_add_i32 s12, s12, s44
	s_add_i32 s14, s14, s44
	s_add_i32 s42, s42, s44
	s_add_i32 s46, s46, s44
	s_add_i32 s52, s52, s44
	s_ashr_i32 s50, s16, 31
	s_lshl_b32 s12, s12, 11
	s_ashr_i32 s51, s18, 31
	s_lshl_b32 s14, s14, 11
	s_ashr_i32 s53, s20, 31
	s_lshl_b32 s42, s42, 11
	s_ashr_i32 s54, s22, 31
	s_lshl_b32 s46, s46, 11
	s_ashr_i32 s55, s24, 31
	s_ashr_i32 s56, s26, 31
	s_ashr_i32 s57, s28, 31
	s_lshl_b32 s72, s52, 11
	s_ashr_i32 s58, s30, 31
	s_lshl_b64 s[60:61], s[40:41], 2
	v_readlane_b32 s44, v252, 38
	s_add_u32 s52, s44, s60
	v_readlane_b32 s45, v252, 40
	s_addc_u32 s60, s45, s61
	s_lshl_b64 s[10:11], s[10:11], 2
	s_mov_b32 s13, s79
	s_add_u32 s59, s52, s10
	s_addc_u32 s60, s60, s11
	s_lshl_b64 s[12:13], s[12:13], 2
	s_add_u32 s12, s44, s12
	s_addc_u32 s13, s45, s13
	s_and_b32 s52, s19, 0x1c00
	s_mov_b32 s15, s79
	s_add_u32 s61, s12, s52
	s_addc_u32 s62, s13, 0
	s_lshl_b64 s[12:13], s[14:15], 2
	s_add_u32 s12, s44, s12
	s_addc_u32 s13, s45, s13
	s_and_b32 s14, s21, 0x1c00
	s_mov_b32 s43, s79
	s_add_u32 s63, s12, s14
	s_addc_u32 s64, s13, 0
	s_lshl_b64 s[12:13], s[42:43], 2
	s_add_u32 s12, s44, s12
	s_addc_u32 s13, s45, s13
	s_and_b32 s14, s23, 0x1c00
	s_mov_b32 s47, s79
	s_add_u32 s65, s12, s14
	s_addc_u32 s66, s13, 0
	s_lshl_b64 s[12:13], s[46:47], 2
	s_add_u32 s12, s44, s12
	s_addc_u32 s13, s45, s13
	s_and_b32 s14, s25, 0x1c00
	s_mov_b32 s69, s79
	s_add_u32 s67, s12, s14
	s_addc_u32 s86, s13, 0
	s_lshl_b64 s[12:13], s[68:69], 2
	s_add_u32 s12, s44, s12
	s_addc_u32 s13, s45, s13
	s_and_b32 s14, s27, 0x1c00
	s_mov_b32 s71, s79
	s_add_u32 s87, s12, s14
	s_addc_u32 s94, s13, 0
	s_lshl_b64 s[12:13], s[70:71], 2
	s_add_u32 s12, s44, s12
	s_addc_u32 s13, s45, s13
	s_and_b32 s14, s29, 0x1c00
	s_mov_b32 s73, s79
	s_add_u32 s95, s12, s14
	s_addc_u32 s96, s13, 0
	s_lshl_b64 s[12:13], s[72:73], 2
	s_add_u32 s12, s44, s12
	s_addc_u32 s13, s45, s13
	s_and_b32 s14, s31, 0x1c00
	s_add_u32 s97, s12, s14
	s_addc_u32 s42, s13, 0
	s_lshl_b64 s[8:9], s[8:9], 2
	s_add_u32 s8, s44, s8
	s_addc_u32 s9, s45, s9
	s_add_u32 s43, s8, s10
	s_addc_u32 s52, s9, s11
	s_lshl_b32 s8, s74, 6
	v_readlane_b32 s9, v252, 52
	v_and_b32_e32 v66, 31, v66
	s_add_u32 s8, s9, s8
	v_readlane_b32 s9, v252, 55
	v_lshrrev_b32_e32 v135, 5, v67
	v_readlane_b32 s40, v252, 16
	s_addc_u32 s9, s9, 0
	v_lshlrev_b32_e32 v66, 1, v66
	v_mov_b32_e32 v67, v131
	v_readlane_b32 s72, v252, 50
	v_mov_b32_e32 v3, v2
	v_mov_b32_e32 v4, v2
	v_mov_b32_e32 v5, v2
	v_mov_b32_e32 v6, v2
	v_mov_b32_e32 v7, v2
	v_mov_b32_e32 v8, v2
	v_mov_b32_e32 v9, v2
	v_mov_b32_e32 v10, v2
	v_mov_b32_e32 v11, v2
	v_mov_b32_e32 v12, v2
	v_mov_b32_e32 v13, v2
	v_mov_b32_e32 v14, v2
	v_mov_b32_e32 v15, v2
	v_mov_b32_e32 v16, v2
	v_mov_b32_e32 v17, v2
	v_mov_b32_e32 v19, v18
	v_mov_b32_e32 v20, v18
	v_mov_b32_e32 v21, v18
	v_mov_b32_e32 v22, v18
	v_mov_b32_e32 v23, v18
	v_mov_b32_e32 v24, v18
	v_mov_b32_e32 v25, v18
	v_mov_b32_e32 v26, v18
	v_mov_b32_e32 v27, v18
	v_mov_b32_e32 v28, v18
	v_mov_b32_e32 v29, v18
	v_mov_b32_e32 v30, v18
	v_mov_b32_e32 v31, v18
	v_mov_b32_e32 v32, v18
	v_mov_b32_e32 v33, v18
	v_mov_b32_e32 v35, v34
	v_mov_b32_e32 v36, v34
	v_mov_b32_e32 v37, v34
	v_mov_b32_e32 v38, v34
	v_mov_b32_e32 v39, v34
	v_mov_b32_e32 v40, v34
	v_mov_b32_e32 v41, v34
	v_mov_b32_e32 v42, v34
	v_mov_b32_e32 v43, v34
	v_mov_b32_e32 v44, v34
	v_mov_b32_e32 v45, v34
	v_mov_b32_e32 v46, v34
	v_mov_b32_e32 v47, v34
	v_mov_b32_e32 v48, v34
	v_mov_b32_e32 v49, v34
	v_mov_b32_e32 v51, v50
	v_mov_b32_e32 v52, v50
	v_mov_b32_e32 v53, v50
	v_mov_b32_e32 v54, v50
	v_mov_b32_e32 v55, v50
	v_mov_b32_e32 v56, v50
	v_mov_b32_e32 v57, v50
	v_mov_b32_e32 v58, v50
	v_mov_b32_e32 v59, v50
	v_mov_b32_e32 v60, v50
	v_mov_b32_e32 v61, v50
	v_mov_b32_e32 v62, v50
	v_mov_b32_e32 v63, v50
	v_mov_b32_e32 v64, v50
	v_mov_b32_e32 v65, v50
	v_add_u32_e32 v136, 0, v130
	v_readlane_b32 s41, v252, 17
	v_lshl_add_u64 v[132:133], s[8:9], 0, v[66:67]
	s_mov_b32 s46, 34
	s_mov_b32 s47, -4
	s_waitcnt vmcnt(0)
	v_mov_b32_e32 v137, v134
	v_readlane_b32 s44, v252, 37
	v_readlane_b32 s73, v252, 51
	v_readlane_b32 s45, v252, 46
	v_readlane_b32 s71, v252, 47
	v_readlane_b32 s74, v252, 48
	s_lshl_b32 s10, s16, 10
	s_add_u32 s10, s40, s10
	s_addc_u32 s11, s41, 0
	s_cmp_lg_u64 s[0:1], 0
	s_cselect_b32 s59, s59, s10
	s_cselect_b32 s60, s60, s11
	s_lshl_b32 s10, s18, 10
	s_add_u32 s10, s40, s10
	s_addc_u32 s11, s41, 0
	s_cmp_lg_u64 s[0:1], 0
	s_cselect_b32 s61, s61, s10
	s_cselect_b32 s62, s62, s11
	s_lshl_b32 s10, s20, 10
	s_add_u32 s10, s40, s10
	s_addc_u32 s11, s41, 0
	s_cmp_eq_u64 s[4:5], 0
	s_cselect_b32 s63, s63, s10
	s_cselect_b32 s64, s64, s11
	s_lshl_b32 s10, s22, 10
	s_add_u32 s10, s40, s10
	s_addc_u32 s11, s41, 0
	s_cmp_eq_u64 s[4:5], 0
	s_cselect_b32 s65, s65, s10
	s_cselect_b32 s66, s66, s11
	s_lshl_b32 s10, s24, 10
	s_add_u32 s10, s40, s10
	s_addc_u32 s11, s41, 0
	s_cmp_eq_u64 s[4:5], 0
	s_cselect_b32 s67, s67, s10
	s_cselect_b32 s86, s86, s11
	s_lshl_b32 s10, s26, 10
	s_add_u32 s10, s40, s10
	s_addc_u32 s11, s41, 0
	s_cmp_eq_u64 s[4:5], 0
	s_cselect_b32 s87, s87, s10
	s_cselect_b32 s94, s94, s11
	s_lshl_b32 s10, s28, 10
	s_add_u32 s10, s40, s10
	s_addc_u32 s11, s41, 0
	s_cmp_eq_u64 s[4:5], 0
	s_cselect_b32 s95, s95, s10
	s_cselect_b32 s96, s96, s11
	s_lshl_b32 s10, s30, 10
	s_add_u32 s10, s40, s10
	s_addc_u32 s11, s41, 0
	s_cmp_eq_u64 s[4:5], 0
	s_cselect_b32 s97, s97, s10
	s_cselect_b32 s42, s42, s11
	s_lshl_b32 s10, s36, 10
	s_add_u32 s10, s40, s10
	s_addc_u32 s11, s41, 0
	s_cmp_eq_u64 s[4:5], 0
	s_cselect_b32 s43, s43, s10
	s_cselect_b32 s52, s52, s11
	s_branch .LBB0_716
.LBB0_714:
	s_ashr_i32 s9, s11, 31
	v_readlane_b32 s8, v252, 49
	s_add_u32 s8, s8, s11
	v_mov_b32_e32 v100, v135
	s_addc_u32 s9, 0, s9
	s_lshl_b64 s[8:9], s[8:9], 10
	v_mul_lo_u32 v100, s74, v100
	v_lshl_add_u64 v[98:99], v[132:133], 0, s[8:9]
	v_ashrrev_i32_e32 v101, 31, v100
	v_readlane_b32 s8, v254, 48
	v_lshl_add_u64 v[98:99], v[100:101], 1, v[98:99]
	v_readlane_b32 s9, v254, 49
	v_cvt_pk_bf16_f32 v100, v82, v83
	v_cvt_pk_bf16_f32 v84, v84, v85
	v_lshl_add_u64 v[82:83], s[8:9], 1, v[98:99]
	v_readlane_b32 s8, v254, 40
	v_readlane_b32 s9, v254, 41
	global_store_short_d16_hi v[82:83], v100, off
	v_readlane_b32 s10, v254, 50
	v_lshl_add_u64 v[82:83], v[82:83], 0, s[8:9]
	global_store_short v[82:83], v84, off
	v_lshl_add_u64 v[82:83], v[82:83], 0, s[8:9]
	v_readlane_b32 s11, v254, 51
	global_store_short_d16_hi v[82:83], v84, off
	v_cvt_pk_bf16_f32 v84, v86, v87
	v_lshl_add_u64 v[82:83], v[82:83], 0, s[10:11]
	global_store_short v[82:83], v84, off
	v_lshl_add_u64 v[82:83], v[82:83], 0, s[8:9]
	global_store_short v[98:99], v100, off
	global_store_short_d16_hi v[82:83], v84, off
	v_cvt_pk_bf16_f32 v84, v88, v89
	v_lshl_add_u64 v[82:83], v[82:83], 0, s[8:9]
	global_store_short v[82:83], v84, off
	v_lshl_add_u64 v[82:83], v[82:83], 0, s[8:9]
	global_store_short_d16_hi v[82:83], v84, off
	v_cvt_pk_bf16_f32 v84, v90, v91
	v_lshl_add_u64 v[82:83], v[82:83], 0, s[10:11]
	global_store_short v[82:83], v84, off
	v_lshl_add_u64 v[82:83], v[82:83], 0, s[8:9]
	global_store_short_d16_hi v[82:83], v84, off
	v_cvt_pk_bf16_f32 v84, v92, v93
	v_lshl_add_u64 v[82:83], v[82:83], 0, s[8:9]
	global_store_short v[82:83], v84, off
	v_lshl_add_u64 v[82:83], v[82:83], 0, s[8:9]
	global_store_short_d16_hi v[82:83], v84, off
	v_cvt_pk_bf16_f32 v84, v94, v95
	v_lshl_add_u64 v[82:83], v[82:83], 0, s[10:11]
	global_store_short v[82:83], v84, off
	v_lshl_add_u64 v[82:83], v[82:83], 0, s[8:9]
	global_store_short_d16_hi v[82:83], v84, off
	v_cvt_pk_bf16_f32 v84, v96, v97
	v_lshl_add_u64 v[82:83], v[82:83], 0, s[8:9]
	global_store_short v[82:83], v84, off
	v_lshl_add_u64 v[82:83], v[82:83], 0, s[8:9]
	global_store_short_d16_hi v[82:83], v84, off
	v_cvt_pk_bf16_f32 v84, v66, v67
	v_lshl_add_u64 v[66:67], v[82:83], 0, s[10:11]
	global_store_short v[66:67], v84, off
	v_lshl_add_u64 v[66:67], v[66:67], 0, s[8:9]
	global_store_short_d16_hi v[66:67], v84, off
	v_cvt_pk_bf16_f32 v68, v68, v69
	v_lshl_add_u64 v[66:67], v[66:67], 0, s[8:9]
	global_store_short v[66:67], v68, off
	v_lshl_add_u64 v[66:67], v[66:67], 0, s[8:9]
	global_store_short_d16_hi v[66:67], v68, off
	v_cvt_pk_bf16_f32 v68, v70, v71
	v_lshl_add_u64 v[66:67], v[66:67], 0, s[10:11]
	global_store_short v[66:67], v68, off
	v_lshl_add_u64 v[66:67], v[66:67], 0, s[8:9]
	global_store_short_d16_hi v[66:67], v68, off
	v_cvt_pk_bf16_f32 v68, v72, v73
	v_lshl_add_u64 v[66:67], v[66:67], 0, s[8:9]
	global_store_short v[66:67], v68, off
	v_lshl_add_u64 v[66:67], v[66:67], 0, s[8:9]
	global_store_short_d16_hi v[66:67], v68, off
	v_cvt_pk_bf16_f32 v68, v74, v75
	v_lshl_add_u64 v[66:67], v[66:67], 0, s[10:11]
	global_store_short v[66:67], v68, off
	v_lshl_add_u64 v[66:67], v[66:67], 0, s[8:9]
	global_store_short_d16_hi v[66:67], v68, off
	v_cvt_pk_bf16_f32 v68, v76, v77
	v_lshl_add_u64 v[66:67], v[66:67], 0, s[8:9]
	global_store_short v[66:67], v68, off
	v_lshl_add_u64 v[66:67], v[66:67], 0, s[8:9]
	global_store_short_d16_hi v[66:67], v68, off
	v_cvt_pk_bf16_f32 v68, v78, v79
	v_lshl_add_u64 v[66:67], v[66:67], 0, s[10:11]
	global_store_short v[66:67], v68, off
	v_lshl_add_u64 v[66:67], v[66:67], 0, s[8:9]
	global_store_short_d16_hi v[66:67], v68, off
	v_cvt_pk_bf16_f32 v68, v80, v81
	v_lshl_add_u64 v[66:67], v[66:67], 0, s[8:9]
	global_store_short v[66:67], v68, off
	v_lshl_add_u64 v[66:67], v[66:67], 0, s[8:9]
	global_store_short_d16_hi v[66:67], v68, off
	s_add_i32 s46, s46, -1
	s_add_i32 s47, s47, 1
	s_cmp_lg_u32 s47, 32
	s_waitcnt vmcnt(32)
	v_mov_b32_e32 v134, v137
	s_cbranch_scc0 .LBB0_773
	s_add_i32 s68, s47, 4
	s_branch .Lscan_top

.Lscan_top:
	s_add_i32 s70, s47, 5
	s_cmp_lg_u32 s47, 31
	s_cselect_b64 s[8:9], -1, 0
	s_cmp_eq_u32 s47, 31
	s_waitcnt lgkmcnt(0)
	s_barrier
	s_cbranch_scc0 .LBB0_719
	s_andn2_b64 vcc, exec, s[8:9]
	s_cbranch_vccz .LBB0_724

.LBB0_728:
	s_lshl_b32 s8, s10, 3
	s_add_i32 s12, s8, s45
	s_ashr_i32 s13, s12, 31
	s_lshl_b64 s[8:9], s[12:13], 15
	s_mul_i32 s14, s12, 0xe000
	s_bitcmp1_b32 s70, 0
	s_cselect_b32 s15, 0x12000, 0
	s_cmp_lg_u64 s[0:1], 0
	s_cselect_b32 s13, s8, s14
	s_cmp_lg_u64 s[4:5], 0
	s_cselect_b32 s69, s14, s8
	s_add_u32 s10, s59, s13
	s_addc_u32 s11, s60, 0
	s_add_i32 m0, s15, s17
	v_lshl_add_u64 v[66:67], s[10:11], 0, v[130:131]
	global_load_lds_dwordx4 v[66:67], off
	s_add_u32 s10, s61, s13
	s_addc_u32 s11, s62, 0
	s_add_i32 m0, s15, s19
	v_lshl_add_u64 v[66:67], s[10:11], 0, v[130:131]
	global_load_lds_dwordx4 v[66:67], off
	s_add_u32 s10, s63, s69
	s_addc_u32 s11, s64, 0
	s_add_i32 m0, s15, s21
	v_lshl_add_u64 v[66:67], s[10:11], 0, v[130:131]
	global_load_lds_dwordx4 v[66:67], off
	s_add_u32 s10, s65, s69
	s_addc_u32 s11, s66, 0
	s_add_i32 m0, s15, s23
	v_lshl_add_u64 v[66:67], s[10:11], 0, v[130:131]
	global_load_lds_dwordx4 v[66:67], off
	s_add_u32 s10, s67, s69
	s_addc_u32 s11, s86, 0
	s_add_i32 m0, s15, s25
	v_lshl_add_u64 v[66:67], s[10:11], 0, v[130:131]
	global_load_lds_dwordx4 v[66:67], off
	s_add_u32 s10, s87, s69
	s_addc_u32 s11, s94, 0
	s_add_i32 m0, s15, s27
	v_lshl_add_u64 v[66:67], s[10:11], 0, v[130:131]
	global_load_lds_dwordx4 v[66:67], off
	s_add_u32 s10, s95, s69
	s_addc_u32 s11, s96, 0
	s_add_i32 m0, s15, s29
	v_lshl_add_u64 v[66:67], s[10:11], 0, v[130:131]
	global_load_lds_dwordx4 v[66:67], off
	s_add_u32 s10, s97, s69
	s_addc_u32 s11, s42, 0
	s_add_i32 m0, s15, s31
	v_lshl_add_u64 v[66:67], s[10:11], 0, v[130:131]
	global_load_lds_dwordx4 v[66:67], off
	s_add_u32 s10, s43, s69
	s_addc_u32 s11, s52, 0
	s_add_i32 m0, s15, s48
	v_lshl_add_u64 v[66:67], s[10:11], 0, v[130:131]
	global_load_lds_dwordx4 v[66:67], off
	s_andn2_b64 vcc, exec, s[6:7]
	s_cbranch_vccnz .LBB0_715

.LBB0_769:
	s_bitcmp1_b32 s68, 0
	s_cselect_b32 s8, 0x12000, 0
	v_add_u32_e32 v190, s8, v136
	v_mov_b32 v82, 0
	v_mov_b32 v66, 0
	ds_read_b128 v[98:101], v190
	ds_read_b128 v[138:141], v190 offset:1024
	ds_read_b128 v[102:105], v190 offset:16384
	ds_read_b128 v[142:145], v190 offset:17408
	ds_read_b128 v[146:149], v190 offset:8192
	ds_read_b128 v[150:153], v190 offset:9216
	ds_read_b128 v[154:157], v190 offset:24576
	ds_read_b128 v[158:161], v190 offset:25600
	v_mov_b32_e32 v83, v82
	v_mov_b32_e32 v84, v82
	v_mov_b32_e32 v85, v82
	v_mov_b32_e32 v86, v82
	v_mov_b32_e32 v87, v82
	v_mov_b32_e32 v88, v82
	v_mov_b32_e32 v89, v82
	v_mov_b32_e32 v90, v82
	v_mov_b32_e32 v91, v82
	v_mov_b32_e32 v92, v82
	v_mov_b32_e32 v93, v82
	v_mov_b32_e32 v94, v82
	v_mov_b32_e32 v95, v82
	v_mov_b32_e32 v96, v82
	v_mov_b32_e32 v97, v82
	v_mov_b32_e32 v67, v66
	v_mov_b32_e32 v68, v66
	v_mov_b32_e32 v69, v66
	v_mov_b32_e32 v70, v66
	v_mov_b32_e32 v71, v66
	v_mov_b32_e32 v72, v66
	v_mov_b32_e32 v73, v66
	v_mov_b32_e32 v74, v66
	v_mov_b32_e32 v75, v66
	v_mov_b32_e32 v76, v66
	v_mov_b32_e32 v77, v66
	v_mov_b32_e32 v78, v66
	v_mov_b32_e32 v79, v66
	v_mov_b32_e32 v80, v66
	v_mov_b32_e32 v81, v66
	v_add_u32_e32 v191, s49, v190
	ds_read_b128 v[162:165], v190 offset:2048
	ds_read_b128 v[166:169], v190 offset:3072
	ds_read_b128 v[170:173], v190 offset:18432
	ds_read_b128 v[174:177], v190 offset:19456
	ds_read_b128 v[178:181], v190 offset:10240
	ds_read_b128 v[182:185], v190 offset:11264
	ds_read_b128 v[186:189], v190 offset:26624
	ds_read_b128 v[198:201], v190 offset:27648
	v_cvt_pk_bf16_f32 v202, v2, v3
	v_cvt_pk_bf16_f32 v203, v4, v5
	v_cvt_pk_bf16_f32 v204, v6, v7
	v_cvt_pk_bf16_f32 v205, v8, v9
	s_waitcnt lgkmcnt(8)
	s_nop 0
	v_mfma_f32_32x32x16_bf16 v[114:129], v[98:101], v[202:205], v[82:97]
	v_mfma_f32_32x32x16_bf16 v[82:97], v[102:105], v[202:205], v[82:97]
	v_mfma_f32_32x32x16_bf16 v[98:113], v[146:149], v[202:205], v[66:81]
	v_cvt_pk_bf16_f32 v146, v10, v11
	v_cvt_pk_bf16_f32 v147, v12, v13
	v_cvt_pk_bf16_f32 v148, v14, v15
	v_cvt_pk_bf16_f32 v149, v16, v17
	v_mfma_f32_32x32x16_bf16 v[66:81], v[154:157], v[202:205], v[66:81]
	s_nop 0
	v_mfma_f32_32x32x16_bf16 v[82:97], v[142:145], v[146:149], v[82:97]
	v_mfma_f32_32x32x16_bf16 v[66:81], v[158:161], v[146:149], v[66:81]
	v_mfma_f32_32x32x16_bf16 v[114:129], v[138:141], v[146:149], v[114:129]
	v_mfma_f32_32x32x16_bf16 v[98:113], v[150:153], v[146:149], v[98:113]
	ds_read_b128 v[138:141], v190 offset:4096
	ds_read_b128 v[142:145], v190 offset:5120
	ds_read_b128 v[146:149], v190 offset:20480
	ds_read_b128 v[150:153], v190 offset:21504
	ds_read_b128 v[154:157], v190 offset:12288
	ds_read_b128 v[158:161], v190 offset:13312
	ds_read_b128 v[202:205], v190 offset:28672
	ds_read_b128 v[206:209], v190 offset:29696
	v_cvt_pk_bf16_f32 v210, v18, v19
	v_cvt_pk_bf16_f32 v211, v20, v21
	v_cvt_pk_bf16_f32 v212, v22, v23
	v_cvt_pk_bf16_f32 v213, v24, v25
	s_waitcnt lgkmcnt(8)
	s_nop 0
	v_mfma_f32_32x32x16_bf16 v[82:97], v[170:173], v[210:213], v[82:97]
	v_mfma_f32_32x32x16_bf16 v[66:81], v[186:189], v[210:213], v[66:81]
	v_mfma_f32_32x32x16_bf16 v[114:129], v[162:165], v[210:213], v[114:129]
	v_cvt_pk_bf16_f32 v162, v26, v27
	v_cvt_pk_bf16_f32 v163, v28, v29
	v_cvt_pk_bf16_f32 v164, v30, v31
	v_cvt_pk_bf16_f32 v165, v32, v33
	v_mfma_f32_32x32x16_bf16 v[98:113], v[178:181], v[210:213], v[98:113]
	s_nop 0
	v_mfma_f32_32x32x16_bf16 v[82:97], v[174:177], v[162:165], v[82:97]
	v_mfma_f32_32x32x16_bf16 v[66:81], v[198:201], v[162:165], v[66:81]
	v_mfma_f32_32x32x16_bf16 v[114:129], v[166:169], v[162:165], v[114:129]
	v_mfma_f32_32x32x16_bf16 v[98:113], v[182:185], v[162:165], v[98:113]
	ds_read_b128 v[162:165], v190 offset:6144
	ds_read_b128 v[166:169], v190 offset:7168
	ds_read_b128 v[170:173], v190 offset:22528
	ds_read_b128 v[174:177], v190 offset:23552
	ds_read_b128 v[178:181], v190 offset:14336
	ds_read_b128 v[182:185], v190 offset:15360
	ds_read_b128 v[186:189], v190 offset:30720
	ds_read_b128 v[198:201], v190 offset:31744
	v_cvt_pk_bf16_f32 v210, v34, v35
	v_cvt_pk_bf16_f32 v211, v36, v37
	v_cvt_pk_bf16_f32 v212, v38, v39
	v_cvt_pk_bf16_f32 v213, v40, v41
	s_waitcnt lgkmcnt(8)
	s_nop 0
	v_mfma_f32_32x32x16_bf16 v[82:97], v[146:149], v[210:213], v[82:97]
	v_mfma_f32_32x32x16_bf16 v[66:81], v[202:205], v[210:213], v[66:81]
	v_mfma_f32_32x32x16_bf16 v[114:129], v[138:141], v[210:213], v[114:129]
	v_cvt_pk_bf16_f32 v138, v42, v43
	v_cvt_pk_bf16_f32 v139, v44, v45
	v_cvt_pk_bf16_f32 v140, v46, v47
	v_cvt_pk_bf16_f32 v141, v48, v49
	v_mfma_f32_32x32x16_bf16 v[98:113], v[154:157], v[210:213], v[98:113]
	s_nop 0
	v_mfma_f32_32x32x16_bf16 v[82:97], v[150:153], v[138:141], v[82:97]
	v_mfma_f32_32x32x16_bf16 v[66:81], v[206:209], v[138:141], v[66:81]
	v_mfma_f32_32x32x16_bf16 v[114:129], v[142:145], v[138:141], v[114:129]
	v_mfma_f32_32x32x16_bf16 v[98:113], v[158:161], v[138:141], v[98:113]
	ds_read_b128 v[138:141], v191 offset:57344
	ds_read_b128 v[142:145], v191 offset:58368
	ds_read_b128 v[146:149], v191 offset:59392
	ds_read_b128 v[150:153], v191 offset:60416
	ds_read_b128 v[154:157], v191 offset:61440
	ds_read_b128 v[158:161], v191 offset:62464
	ds_read_b128 v[202:205], v191 offset:63488
	ds_read_b128 v[206:209], v191 offset:64512
	v_cvt_pk_bf16_f32 v210, v50, v51
	v_cvt_pk_bf16_f32 v211, v52, v53
	v_cvt_pk_bf16_f32 v212, v54, v55
	v_cvt_pk_bf16_f32 v213, v56, v57
	s_waitcnt lgkmcnt(8)
	s_nop 0
	v_mfma_f32_32x32x16_bf16 v[82:97], v[170:173], v[210:213], v[82:97]
	v_mfma_f32_32x32x16_bf16 v[66:81], v[186:189], v[210:213], v[66:81]
	v_mfma_f32_32x32x16_bf16 v[114:129], v[162:165], v[210:213], v[114:129]
	v_cvt_pk_bf16_f32 v162, v58, v59
	v_cvt_pk_bf16_f32 v163, v60, v61
	v_cvt_pk_bf16_f32 v164, v62, v63
	v_cvt_pk_bf16_f32 v165, v64, v65
	v_mfma_f32_32x32x16_bf16 v[98:113], v[178:181], v[210:213], v[98:113]
	s_nop 0
	v_mfma_f32_32x32x16_bf16 v[82:97], v[174:177], v[162:165], v[82:97]
	v_mfma_f32_32x32x16_bf16 v[66:81], v[198:201], v[162:165], v[66:81]
	v_mfma_f32_32x32x16_bf16 v[114:129], v[166:169], v[162:165], v[114:129]
	v_mfma_f32_32x32x16_bf16 v[98:113], v[182:185], v[162:165], v[98:113]
	ds_read_b128 v[162:165], v190 offset:32768
	ds_read_b128 v[166:169], v190 offset:33792
	ds_read_b128 v[170:173], v190 offset:34816
	ds_read_b128 v[174:177], v190 offset:35840
	ds_read_b128 v[178:181], v190 offset:36864
	ds_read_b128 v[182:185], v190 offset:37888
	ds_read_b128 v[186:189], v190 offset:38912
	ds_read_b128 v[198:201], v190 offset:39936
	s_waitcnt lgkmcnt(8)
	s_nop 1
	v_pk_add_f32 v[114:115], v[138:139], v[114:115] neg_lo:[0,1] neg_hi:[0,1]
	v_pk_add_f32 v[116:117], v[140:141], v[116:117] neg_lo:[0,1] neg_hi:[0,1]
	v_pk_add_f32 v[118:119], v[142:143], v[118:119] neg_lo:[0,1] neg_hi:[0,1]
	v_pk_add_f32 v[122:123], v[146:147], v[122:123] neg_lo:[0,1] neg_hi:[0,1]
	v_pk_add_f32 v[120:121], v[144:145], v[120:121] neg_lo:[0,1] neg_hi:[0,1]
	v_pk_add_f32 v[124:125], v[148:149], v[124:125] neg_lo:[0,1] neg_hi:[0,1]
	v_pk_add_f32 v[126:127], v[150:151], v[126:127] neg_lo:[0,1] neg_hi:[0,1]
	v_cvt_pk_bf16_f32 v114, v114, v115
	v_cvt_pk_bf16_f32 v115, v116, v117
	v_cvt_pk_bf16_f32 v116, v118, v119
	v_cvt_pk_bf16_f32 v118, v122, v123
	v_pk_add_f32 v[122:123], v[152:153], v[128:129] neg_lo:[0,1] neg_hi:[0,1]
	v_pk_add_f32 v[98:99], v[154:155], v[98:99] neg_lo:[0,1] neg_hi:[0,1]
	v_pk_add_f32 v[100:101], v[156:157], v[100:101] neg_lo:[0,1] neg_hi:[0,1]
	v_pk_add_f32 v[102:103], v[158:159], v[102:103] neg_lo:[0,1] neg_hi:[0,1]
	v_pk_add_f32 v[104:105], v[160:161], v[104:105] neg_lo:[0,1] neg_hi:[0,1]
	v_pk_add_f32 v[106:107], v[202:203], v[106:107] neg_lo:[0,1] neg_hi:[0,1]
	v_pk_add_f32 v[108:109], v[204:205], v[108:109] neg_lo:[0,1] neg_hi:[0,1]
	v_pk_add_f32 v[110:111], v[206:207], v[110:111] neg_lo:[0,1] neg_hi:[0,1]
	v_sub_f32_e32 v113, v209, v113
	v_sub_f32_e32 v112, v208, v112
	v_cvt_pk_bf16_f32 v117, v120, v121
	v_cvt_pk_bf16_f32 v119, v124, v125
	v_cvt_pk_bf16_f32 v120, v126, v127
	v_cvt_pk_bf16_f32 v121, v122, v123
	v_cvt_pk_bf16_f32 v98, v98, v99
	v_cvt_pk_bf16_f32 v99, v100, v101
	v_cvt_pk_bf16_f32 v100, v102, v103
	v_cvt_pk_bf16_f32 v101, v104, v105
	v_cvt_pk_bf16_f32 v102, v106, v107
	v_cvt_pk_bf16_f32 v103, v108, v109
	v_cvt_pk_bf16_f32 v104, v110, v111
	v_cvt_pk_bf16_f32 v105, v112, v113
	ds_read_b128 v[106:109], v190 offset:40960
	ds_read_b128 v[110:113], v190 offset:41984
	ds_read_b128 v[122:125], v190 offset:43008
	ds_read_b128 v[126:129], v190 offset:44032
	ds_read_b128 v[138:141], v190 offset:45056
	ds_read_b128 v[142:145], v190 offset:46080
	ds_read_b128 v[146:149], v190 offset:47104
	ds_read_b128 v[150:153], v190 offset:48128
	s_waitcnt lgkmcnt(8)
	v_mfma_f32_32x32x16_bf16 v[82:97], v[162:165], v[114:117], v[82:97]
	v_mfma_f32_32x32x16_bf16 v[66:81], v[178:181], v[114:117], v[66:81]
	v_mfma_f32_32x32x16_bf16 v[82:97], v[166:169], v[118:121], v[82:97]
	v_mfma_f32_32x32x16_bf16 v[66:81], v[182:185], v[118:121], v[66:81]
	v_mfma_f32_32x32x16_bf16 v[82:97], v[170:173], v[98:101], v[82:97]
	v_mfma_f32_32x32x16_bf16 v[66:81], v[186:189], v[98:101], v[66:81]
	v_mfma_f32_32x32x16_bf16 v[82:97], v[174:177], v[102:105], v[82:97]
	v_mfma_f32_32x32x16_bf16 v[66:81], v[198:201], v[102:105], v[66:81]
	ds_read_b128 v[154:157], v190 offset:49152
	ds_read_b128 v[158:161], v190 offset:50176
	ds_read_b128 v[162:165], v190 offset:51200
	ds_read_b128 v[166:169], v190 offset:52224
	ds_read_b128 v[170:173], v190 offset:53248
	ds_read_b128 v[174:177], v190 offset:54272
	ds_read_b128 v[178:181], v190 offset:55296
	ds_read_b128 v[182:185], v190 offset:56320
	v_pk_mul_f32 v[16:17], v[16:17], v[134:135] op_sel_hi:[1,0]
	v_pk_mul_f32 v[14:15], v[14:15], v[134:135] op_sel_hi:[1,0]
	v_pk_mul_f32 v[12:13], v[12:13], v[134:135] op_sel_hi:[1,0]
	v_pk_mul_f32 v[10:11], v[10:11], v[134:135] op_sel_hi:[1,0]
	v_pk_mul_f32 v[8:9], v[8:9], v[134:135] op_sel_hi:[1,0]
	v_pk_mul_f32 v[6:7], v[6:7], v[134:135] op_sel_hi:[1,0]
	v_pk_mul_f32 v[4:5], v[4:5], v[134:135] op_sel_hi:[1,0]
	v_pk_mul_f32 v[2:3], v[2:3], v[134:135] op_sel_hi:[1,0]
	v_pk_mul_f32 v[32:33], v[32:33], v[134:135] op_sel_hi:[1,0]
	v_pk_mul_f32 v[30:31], v[30:31], v[134:135] op_sel_hi:[1,0]
	v_pk_mul_f32 v[28:29], v[28:29], v[134:135] op_sel_hi:[1,0]
	v_pk_mul_f32 v[26:27], v[26:27], v[134:135] op_sel_hi:[1,0]
	v_pk_mul_f32 v[24:25], v[24:25], v[134:135] op_sel_hi:[1,0]
	v_pk_mul_f32 v[22:23], v[22:23], v[134:135] op_sel_hi:[1,0]
	v_pk_mul_f32 v[20:21], v[20:21], v[134:135] op_sel_hi:[1,0]
	v_pk_mul_f32 v[18:19], v[18:19], v[134:135] op_sel_hi:[1,0]
	s_waitcnt lgkmcnt(8)
	v_mfma_f32_32x32x16_bf16 v[2:17], v[106:109], v[114:117], v[2:17]
	v_mfma_f32_32x32x16_bf16 v[18:33], v[138:141], v[114:117], v[18:33]
	v_mfma_f32_32x32x16_bf16 v[2:17], v[110:113], v[118:121], v[2:17]
	v_mfma_f32_32x32x16_bf16 v[18:33], v[142:145], v[118:121], v[18:33]
	v_mfma_f32_32x32x16_bf16 v[2:17], v[122:125], v[98:101], v[2:17]
	v_mfma_f32_32x32x16_bf16 v[18:33], v[146:149], v[98:101], v[18:33]
	v_mfma_f32_32x32x16_bf16 v[2:17], v[126:129], v[102:105], v[2:17]
	v_mfma_f32_32x32x16_bf16 v[18:33], v[150:153], v[102:105], v[18:33]
	v_mul_f32_e64 v48, v48, v134
	v_mul_f32_e64 v49, v49, v134
	v_mul_f32_e64 v46, v46, v134
	v_mul_f32_e64 v47, v47, v134
	v_mul_f32_e64 v44, v44, v134
	v_mul_f32_e64 v45, v45, v134
	v_pk_mul_f32 v[42:43], v[42:43], v[134:135] op_sel_hi:[1,0]
	v_pk_mul_f32 v[40:41], v[40:41], v[134:135] op_sel_hi:[1,0]
	v_pk_mul_f32 v[38:39], v[38:39], v[134:135] op_sel_hi:[1,0]
	v_pk_mul_f32 v[36:37], v[36:37], v[134:135] op_sel_hi:[1,0]
	v_pk_mul_f32 v[34:35], v[34:35], v[134:135] op_sel_hi:[1,0]
	v_pk_mul_f32 v[64:65], v[64:65], v[134:135] op_sel_hi:[1,0]
	v_pk_mul_f32 v[62:63], v[62:63], v[134:135] op_sel_hi:[1,0]
	v_pk_mul_f32 v[60:61], v[60:61], v[134:135] op_sel_hi:[1,0]
	v_pk_mul_f32 v[58:59], v[58:59], v[134:135] op_sel_hi:[1,0]
	v_pk_mul_f32 v[56:57], v[56:57], v[134:135] op_sel_hi:[1,0]
	v_pk_mul_f32 v[54:55], v[54:55], v[134:135] op_sel_hi:[1,0]
	v_pk_mul_f32 v[52:53], v[52:53], v[134:135] op_sel_hi:[1,0]
	v_pk_mul_f32 v[50:51], v[50:51], v[134:135] op_sel_hi:[1,0]
	s_waitcnt lgkmcnt(0)
	v_mfma_f32_32x32x16_bf16 v[34:49], v[154:157], v[114:117], v[34:49]
	s_mov_b64 s[8:9], -1
	s_cmpk_gt_i32 s10, 0xff
	v_mfma_f32_32x32x16_bf16 v[50:65], v[170:173], v[114:117], v[50:65]
	v_mfma_f32_32x32x16_bf16 v[34:49], v[158:161], v[118:121], v[34:49]
	v_mfma_f32_32x32x16_bf16 v[50:65], v[174:177], v[118:121], v[50:65]
	v_mfma_f32_32x32x16_bf16 v[34:49], v[162:165], v[98:101], v[34:49]
	v_mfma_f32_32x32x16_bf16 v[50:65], v[178:181], v[98:101], v[50:65]
	v_mfma_f32_32x32x16_bf16 v[34:49], v[166:169], v[102:105], v[34:49]
	v_mfma_f32_32x32x16_bf16 v[50:65], v[182:185], v[102:105], v[50:65]
	s_cbranch_scc0 .LBB0_771
	s_lshl_b32 s11, s10, 6
	s_mov_b64 s[8:9], 0
